# plus nt on conv PROJ loads, P0 f32 weight loads, P6 residual x loads
# baseline (speedup 1.0000x reference)
; #define LAS __attribute__((address_space(3)))
; DI unsigned cvtpk(float lo, float hi) { f32x2 v = {lo, hi}; bf16x2_t b = __builtin_convertvector(v, bf16x2_t); return __builtin_bit_cast(unsigned, b); }
; template <int MODE  >
; DI void p0_tr_item(const float* W, int ld, bf16* WT, int K, int k0, int n0, LAS unsigned char* img, int lane) {
;     ...
;     for (int bt = 0; bt < 4; ++bt) {
;         f32x4 v[8];
; #pragma unroll
;         for (int i = 0; i < 8; ++i) v[i] = *(const f32x4*)(wp + (size_t)(2 * (8 * bt + i)) * ld);
; #pragma unroll
;         for (int i = 0; i < 8; ++i) { const int kk = 2 * (8 * bt + i) + (lane >> 5), n = 4 * (lane & 31);
;             u32x2 pk; pk.x = cvtpk(v[i][0], v[i][1]); pk.y = cvtpk(v[i][2], v[i][3]);
;             *(LAS u32x2*)(img + img_off(kk, n >> 3) + (n & 7) * 2) = pk; }
;     }
.LBB0_36:
	s_waitcnt vmcnt(4)
	v_lshl_add_u64 v[62:63], v[10:11], 0, s[0:1]
	v_add_co_u32_e32 v38, vcc, 0x4000, v62
	global_load_dwordx4 v[34:37], v[62:63], off nt
	s_nop 0
	v_addc_co_u32_e32 v39, vcc, 0, v63, vcc
	s_waitcnt vmcnt(2)
	v_add_co_u32_e32 v42, vcc, 0x8000, v62
	global_load_dwordx4 v[38:41], v[38:39], off nt
	s_nop 0
	v_addc_co_u32_e32 v43, vcc, 0, v63, vcc
	v_add_co_u32_e32 v46, vcc, 0xc000, v62
	v_subrev_u32_e32 v66, 48, v12
	s_nop 0
	v_addc_co_u32_e32 v47, vcc, 0, v63, vcc
	v_add_co_u32_e32 v50, vcc, 0x10000, v62
	global_load_dwordx4 v[42:45], v[42:43], off nt
	s_nop 0
	global_load_dwordx4 v[46:49], v[46:47], off nt
	v_addc_co_u32_e32 v51, vcc, 0, v63, vcc
	v_add_co_u32_e32 v54, vcc, 0x14000, v62
	v_add_u32_e32 v33, v13, v16
	s_nop 0
	v_addc_co_u32_e32 v55, vcc, 0, v63, vcc
	v_add_co_u32_e32 v58, vcc, 0x18000, v62
	global_load_dwordx4 v[50:53], v[50:51], off nt
	s_nop 0
	global_load_dwordx4 v[54:57], v[54:55], off nt
	v_addc_co_u32_e32 v59, vcc, 0, v63, vcc
	v_add_co_u32_e32 v62, vcc, 0x1c000, v62
	global_load_dwordx4 v[58:61], v[58:59], off nt
	s_nop 0
	v_addc_co_u32_e32 v63, vcc, 0, v63, vcc
	global_load_dwordx4 v[62:65], v[62:63], off nt
	v_subrev_u32_e32 v68, 32, v12
	v_bitop3_b32 v66, v66, v15, 12 bitop3:0x6c
	v_and_b32_e32 v68, 12, v68
	v_lshl_add_u32 v66, v66, 4, v13
	v_add_u32_e32 v67, v13, v17
	v_add_u32_e32 v70, -16, v12
	v_bitop3_b32 v68, v68, v15, 1 bitop3:0x36
	v_and_b32_e32 v70, 12, v70
	v_lshl_add_u32 v68, v68, 4, v13
	v_add_u32_e32 v69, v13, v18
	v_bitop3_b32 v70, v70, v15, 2 bitop3:0x36
	v_and_b32_e32 v72, 12, v12
	s_add_u32 s0, s0, 0x20000
	v_lshl_add_u32 v70, v70, 4, v13
	v_add_u32_e32 v71, v13, v19
	v_bitop3_b32 v72, v72, v15, 3 bitop3:0x36
	s_addc_u32 s1, s1, 0
	v_add_u32_e32 v12, 64, v12
	v_lshl_add_u32 v72, v72, 4, v13
	s_cmp_lg_u32 s0, 0x80000
	v_add_u32_e32 v13, 0x1000, v13
	s_waitcnt vmcnt(7)
	v_cvt_pk_bf16_f32 v34, v34, v35
	v_cvt_pk_bf16_f32 v35, v36, v37
	ds_write_b64 v33, v[34:35]
	s_waitcnt vmcnt(6)
	v_cvt_pk_bf16_f32 v34, v38, v39
	v_cvt_pk_bf16_f32 v35, v40, v41
	ds_write_b64 v66, v[34:35] offset:512
	s_waitcnt vmcnt(5)
	v_cvt_pk_bf16_f32 v34, v42, v43
	v_cvt_pk_bf16_f32 v35, v44, v45
	ds_write_b64 v67, v[34:35] offset:1024
	s_waitcnt vmcnt(4)
	v_cvt_pk_bf16_f32 v34, v46, v47
	v_cvt_pk_bf16_f32 v35, v48, v49
	ds_write_b64 v68, v[34:35] offset:1536
	s_waitcnt vmcnt(3)
	v_cvt_pk_bf16_f32 v34, v50, v51
	v_cvt_pk_bf16_f32 v35, v52, v53
	ds_write_b64 v69, v[34:35] offset:2048
	s_waitcnt vmcnt(2)
	v_cvt_pk_bf16_f32 v34, v54, v55
	v_cvt_pk_bf16_f32 v35, v56, v57
	ds_write_b64 v70, v[34:35] offset:2560
	s_waitcnt vmcnt(1)
	v_cvt_pk_bf16_f32 v34, v58, v59
	v_cvt_pk_bf16_f32 v35, v60, v61
	ds_write_b64 v71, v[34:35] offset:3072
	s_waitcnt vmcnt(0)
	v_cvt_pk_bf16_f32 v34, v62, v63
	v_cvt_pk_bf16_f32 v35, v64, v65
	ds_write_b64 v72, v[34:35] offset:3584
	s_cbranch_scc1 .LBB0_36
	s_and_b32 s2, s2, 15
	s_add_i32 s4, s3, 0xffffe800
	s_lshl_b32 s2, s2, 19
	s_lshl_b64 s[0:1], s[4:5], 1
	v_lshl_or_b32 v10, v31, 12, s2
	v_mov_b32_e32 v11, v3
	v_or_b32_e32 v12, s2, v32
	v_mov_b32_e32 v13, v3
	s_waitcnt lgkmcnt(0)
	v_lshl_add_u64 v[10:11], s[0:1], 0, v[10:11]
	v_lshl_add_u64 v[12:13], s[0:1], 0, v[12:13]
	v_lshl_add_u64 v[10:11], v[8:9], 0, v[10:11]
	v_lshl_add_u64 v[12:13], v[8:9], 0, v[12:13]
	s_mov_b64 s[0:1], 0
	v_mov_b32_e32 v33, v1

; #define LAS __attribute__((address_space(3)))
; DI unsigned cvtpk(float lo, float hi) { f32x2 v = {lo, hi}; bf16x2_t b = __builtin_convertvector(v, bf16x2_t); return __builtin_bit_cast(unsigned, b); }
; template <int MODE  >
; DI void p0_tr_item(const float* W, int ld, bf16* WT, int K, int k0, int n0, LAS unsigned char* img, int lane) {
;     ...
;     for (int bt = 0; bt < 4; ++bt) {
;         f32x4 v[8];
; #pragma unroll
;         for (int i = 0; i < 8; ++i) v[i] = *(const f32x4*)(wp + (size_t)(2 * (8 * bt + i)) * ld);
; #pragma unroll
;         for (int i = 0; i < 8; ++i) { const int kk = 2 * (8 * bt + i) + (lane >> 5), n = 4 * (lane & 31);
;             u32x2 pk; pk.x = cvtpk(v[i][0], v[i][1]); pk.y = cvtpk(v[i][2], v[i][3]);
;             *(LAS u32x2*)(img + img_off(kk, n >> 3) + (n & 7) * 2) = pk; }
;     }
.LBB0_42:
	s_waitcnt vmcnt(4)
	v_lshl_add_u64 v[62:63], v[10:11], 0, s[6:7]
	v_add_co_u32_e32 v38, vcc, 0xc000, v62
	global_load_dwordx4 v[34:37], v[62:63], off nt
	s_nop 0
	v_addc_co_u32_e32 v39, vcc, 0, v63, vcc
	s_waitcnt vmcnt(2)
	v_add_co_u32_e32 v42, vcc, 0x18000, v62
	global_load_dwordx4 v[38:41], v[38:39], off offset:64 nt
	s_nop 0
	v_addc_co_u32_e32 v43, vcc, 0, v63, vcc
	v_add_co_u32_e32 v46, vcc, 0x24000, v62
	v_subrev_u32_e32 v66, 48, v12
	s_nop 0
	v_addc_co_u32_e32 v47, vcc, 0, v63, vcc
	v_add_co_u32_e32 v50, vcc, 0x30000, v62
	global_load_dwordx4 v[42:45], v[42:43], off offset:128 nt
	s_nop 0
	global_load_dwordx4 v[46:49], v[46:47], off offset:192 nt
	v_addc_co_u32_e32 v51, vcc, 0, v63, vcc
	v_add_co_u32_e32 v54, vcc, 0x3c000, v62
	v_add_u32_e32 v33, v13, v16
	s_nop 0
	v_addc_co_u32_e32 v55, vcc, 0, v63, vcc
	v_add_co_u32_e32 v58, vcc, 0x48000, v62
	global_load_dwordx4 v[50:53], v[50:51], off offset:256 nt
	s_nop 0
	global_load_dwordx4 v[54:57], v[54:55], off offset:320 nt
	v_addc_co_u32_e32 v59, vcc, 0, v63, vcc
	v_add_co_u32_e32 v62, vcc, 0x54000, v62
	global_load_dwordx4 v[58:61], v[58:59], off offset:384 nt
	s_nop 0
	v_addc_co_u32_e32 v63, vcc, 0, v63, vcc
	global_load_dwordx4 v[62:65], v[62:63], off offset:448 nt
	v_subrev_u32_e32 v68, 32, v12
	v_bitop3_b32 v66, v66, v15, 12 bitop3:0x6c
	v_and_b32_e32 v68, 12, v68
	v_lshl_add_u32 v66, v66, 4, v13
	v_add_u32_e32 v67, v13, v17
	v_add_u32_e32 v70, -16, v12
	v_bitop3_b32 v68, v68, v15, 1 bitop3:0x36
	v_and_b32_e32 v70, 12, v70
	v_lshl_add_u32 v68, v68, 4, v13
	v_add_u32_e32 v69, v13, v18
	v_bitop3_b32 v70, v70, v15, 2 bitop3:0x36
	v_and_b32_e32 v72, 12, v12
	s_add_u32 s6, s6, 0x60200
	v_lshl_add_u32 v70, v70, 4, v13
	v_add_u32_e32 v71, v13, v19
	v_bitop3_b32 v72, v72, v15, 3 bitop3:0x36
	s_addc_u32 s7, s7, 0
	v_add_u32_e32 v12, 64, v12
	v_lshl_add_u32 v72, v72, 4, v13
	s_cmp_lg_u32 s6, 0x180800
	v_add_u32_e32 v13, 0x1000, v13
	s_waitcnt vmcnt(7)
	v_cvt_pk_bf16_f32 v34, v34, v35
	v_cvt_pk_bf16_f32 v35, v36, v37
	ds_write_b64 v33, v[34:35]
	s_waitcnt vmcnt(6)
	v_cvt_pk_bf16_f32 v34, v38, v39
	v_cvt_pk_bf16_f32 v35, v40, v41
	ds_write_b64 v66, v[34:35] offset:512
	s_waitcnt vmcnt(5)
	v_cvt_pk_bf16_f32 v34, v42, v43
	v_cvt_pk_bf16_f32 v35, v44, v45
	ds_write_b64 v67, v[34:35] offset:1024
	s_waitcnt vmcnt(4)
	v_cvt_pk_bf16_f32 v34, v46, v47
	v_cvt_pk_bf16_f32 v35, v48, v49
	ds_write_b64 v68, v[34:35] offset:1536
	s_waitcnt vmcnt(3)
	v_cvt_pk_bf16_f32 v34, v50, v51
	v_cvt_pk_bf16_f32 v35, v52, v53
	ds_write_b64 v69, v[34:35] offset:2048
	s_waitcnt vmcnt(2)
	v_cvt_pk_bf16_f32 v34, v54, v55
	v_cvt_pk_bf16_f32 v35, v56, v57
	ds_write_b64 v70, v[34:35] offset:2560
	s_waitcnt vmcnt(1)
	v_cvt_pk_bf16_f32 v34, v58, v59
	v_cvt_pk_bf16_f32 v35, v60, v61
	ds_write_b64 v71, v[34:35] offset:3072
	s_waitcnt vmcnt(0)
	v_cvt_pk_bf16_f32 v34, v62, v63
	v_cvt_pk_bf16_f32 v35, v64, v65
	ds_write_b64 v72, v[34:35] offset:3584
	s_cbranch_scc1 .LBB0_42
	s_waitcnt lgkmcnt(0)
	s_ashr_i32 s1, s0, 31
	v_or_b32_e32 v10, s2, v20
	v_lshl_add_u64 v[12:13], s[0:1], 1, v[4:5]
	s_mov_b32 s0, 0

; DI void p2_conv(Frame& F, int wk, int nwk) {
;     ...
;     for (int tokb = tok0; tokb < NTOK; tokb += 4 * tstr) {
;         u32x4 raw[4][4];
; #pragma unroll
;         for (int u = 0; u < 4; ++u) { int tok = tokb + u * tstr; tok = tok < NTOK ? tok : NTOK - 1; const int t = tok & (SEQ - 1);
; #pragma unroll
;             for (int j = 0; j < 4; ++j) { const int back = (t - 3 + j < 0) ? t : 3 - j;
;                 raw[u][j] = *(const u32x4*)(PROJ + (size_t)(tok - back) * NPROJ + COL_MQ + c8); } }
.LBB0_233:
	s_waitcnt vmcnt(2)
	v_and_b32_e32 v42, 0x3fff, v1
	v_min_u32_e32 v44, 2, v42
	v_min_u32_e32 v42, 3, v42
	v_sub_u32_e32 v42, v120, v42
	s_waitcnt vmcnt(0)
	v_mov_b64_e32 v[50:51], s[94:95]
	v_mad_i64_i32 v[42:43], s[0:1], v42, s15, v[50:51]
	v_lshl_add_u64 v[42:43], v[42:43], 0, v[106:107]
	v_sub_u32_e32 v44, v120, v44
	v_add_co_u32_e32 v42, vcc, 0x3c001000, v42
	v_mad_i64_i32 v[44:45], s[0:1], v44, s15, v[50:51]
	v_and_b32_e32 v54, 0x3fff, v120
	v_addc_co_u32_e32 v43, vcc, 0, v43, vcc
	v_lshl_add_u64 v[44:45], v[44:45], 0, v[106:107]
	v_add_co_u32_e32 v44, vcc, 0x3c001000, v44
	v_cmp_ne_u32_e64 s[10:11], 0, v54
	s_nop 0
	v_addc_co_u32_e32 v45, vcc, 0, v45, vcc
	global_load_dwordx4 v[94:97], v[42:43], off offset:2048 nt
	global_load_dwordx4 v[90:93], v[44:45], off offset:2048 nt
	v_subbrev_co_u32_e64 v42, vcc, 0, v120, s[10:11]
	v_mad_i64_i32 v[42:43], s[0:1], v42, s15, v[50:51]
	v_lshl_add_u64 v[42:43], v[42:43], 0, v[106:107]
	v_add_co_u32_e32 v42, vcc, 0x3c001000, v42
	v_mad_i64_i32 v[44:45], s[0:1], v120, s15, v[50:51]
	s_nop 0
	v_addc_co_u32_e32 v43, vcc, 0, v43, vcc
	v_lshl_add_u64 v[44:45], v[44:45], 0, v[106:107]
	v_add_co_u32_e32 v44, vcc, 0x3c001000, v44
	v_add_u32_e32 v114, s22, v120
	s_nop 0
	v_addc_co_u32_e32 v45, vcc, 0, v45, vcc
	global_load_dwordx4 v[102:105], v[42:43], off offset:2048 nt
	global_load_dwordx4 v[98:101], v[44:45], off offset:2048 nt
	v_min_i32_e32 v46, 0x7fff, v114
	v_and_b32_e32 v115, 0x3fff, v46
	v_min_u32_e32 v42, 3, v115
	v_sub_u32_e32 v42, v46, v42
	v_mad_i64_i32 v[42:43], s[0:1], v42, s15, v[50:51]
	v_min_u32_e32 v44, 2, v115
	v_lshl_add_u64 v[42:43], v[42:43], 0, v[106:107]
	v_sub_u32_e32 v44, v46, v44
	v_add_co_u32_e32 v42, vcc, s26, v42
	v_mad_i64_i32 v[44:45], s[0:1], v44, s15, v[50:51]
	s_nop 0
	v_addc_co_u32_e32 v43, vcc, 0, v43, vcc
	v_lshl_add_u64 v[44:45], v[44:45], 0, v[106:107]
	v_add_co_u32_e32 v44, vcc, s26, v44
	v_cmp_ne_u32_e64 s[8:9], 0, v115
	s_nop 0
	v_addc_co_u32_e32 v45, vcc, 0, v45, vcc
	global_load_dwordx4 v[78:81], v[42:43], off offset:2048 nt
	global_load_dwordx4 v[74:77], v[44:45], off offset:2048 nt
	v_subbrev_co_u32_e64 v42, vcc, 0, v46, s[8:9]
	v_mad_i64_i32 v[42:43], s[0:1], v42, s15, v[50:51]
	v_lshl_add_u64 v[42:43], v[42:43], 0, v[106:107]
	v_add_co_u32_e32 v42, vcc, s26, v42
	v_mad_i64_i32 v[44:45], s[0:1], v46, s15, v[50:51]
	v_add_u32_e32 v118, s23, v120
	v_addc_co_u32_e32 v43, vcc, 0, v43, vcc
	v_lshl_add_u64 v[44:45], v[44:45], 0, v[106:107]
	v_min_i32_e32 v46, 0x7fff, v118
	v_add_co_u32_e32 v44, vcc, s26, v44
	v_and_b32_e32 v119, 0x3fff, v46
	s_nop 0
	v_addc_co_u32_e32 v45, vcc, 0, v45, vcc
	global_load_dwordx4 v[86:89], v[42:43], off offset:2048 nt
	global_load_dwordx4 v[82:85], v[44:45], off offset:2048 nt
	v_min_u32_e32 v42, 3, v119
	v_sub_u32_e32 v42, v46, v42
	v_mad_i64_i32 v[42:43], s[0:1], v42, s15, v[50:51]
	v_min_u32_e32 v44, 2, v119
	v_lshl_add_u64 v[42:43], v[42:43], 0, v[106:107]
	v_sub_u32_e32 v44, v46, v44
	v_add_co_u32_e32 v42, vcc, s26, v42
	v_mad_i64_i32 v[44:45], s[0:1], v44, s15, v[50:51]
	s_nop 0
	v_addc_co_u32_e32 v43, vcc, 0, v43, vcc
	v_lshl_add_u64 v[44:45], v[44:45], 0, v[106:107]
	v_add_co_u32_e32 v44, vcc, s26, v44
	v_cmp_ne_u32_e64 s[6:7], 0, v119
	s_nop 0
	v_addc_co_u32_e32 v45, vcc, 0, v45, vcc
	global_load_dwordx4 v[62:65], v[42:43], off offset:2048 nt
	global_load_dwordx4 v[58:61], v[44:45], off offset:2048 nt
	v_subbrev_co_u32_e64 v42, vcc, 0, v46, s[6:7]
	v_mad_i64_i32 v[42:43], s[0:1], v42, s15, v[50:51]
	v_lshl_add_u64 v[42:43], v[42:43], 0, v[106:107]
	v_add_co_u32_e32 v42, vcc, s26, v42
	v_mad_i64_i32 v[44:45], s[0:1], v46, s15, v[50:51]
	v_add_u32_e32 v116, s24, v120
	v_addc_co_u32_e32 v43, vcc, 0, v43, vcc
	v_lshl_add_u64 v[44:45], v[44:45], 0, v[106:107]
	v_min_i32_e32 v55, 0x7fff, v116
	v_add_co_u32_e32 v44, vcc, s26, v44
	v_and_b32_e32 v117, 0x3fff, v55
	s_nop 0
	v_addc_co_u32_e32 v45, vcc, 0, v45, vcc
	global_load_dwordx4 v[70:73], v[42:43], off offset:2048 nt
	global_load_dwordx4 v[66:69], v[44:45], off offset:2048 nt
	v_min_u32_e32 v42, 3, v117
	v_sub_u32_e32 v42, v55, v42
	v_mad_i64_i32 v[42:43], s[0:1], v42, s15, v[50:51]
	v_min_u32_e32 v44, 2, v117
	v_lshl_add_u64 v[42:43], v[42:43], 0, v[106:107]
	v_sub_u32_e32 v44, v55, v44
	v_add_co_u32_e32 v42, vcc, s26, v42
	v_mad_i64_i32 v[44:45], s[0:1], v44, s15, v[50:51]
	s_nop 0
	v_addc_co_u32_e32 v43, vcc, 0, v43, vcc
	v_lshl_add_u64 v[44:45], v[44:45], 0, v[106:107]
	v_add_co_u32_e32 v44, vcc, s26, v44
	v_cmp_ne_u32_e64 s[4:5], 0, v117
	s_nop 0
	v_addc_co_u32_e32 v45, vcc, 0, v45, vcc
	v_subbrev_co_u32_e64 v52, vcc, 0, v55, s[4:5]
	v_mad_i64_i32 v[52:53], s[0:1], v52, s15, v[50:51]
	v_lshl_add_u64 v[52:53], v[52:53], 0, v[106:107]
	v_add_co_u32_e32 v52, vcc, s26, v52
	v_mad_i64_i32 v[50:51], s[0:1], v55, s15, v[50:51]
	s_nop 0
	v_addc_co_u32_e32 v53, vcc, 0, v53, vcc
	v_cmp_gt_u32_e32 vcc, 3, v54
	s_waitcnt vmcnt(11)
; DI unsigned cvtpk(float lo, float hi) { f32x2 v = {lo, hi}; bf16x2_t b = __builtin_convertvector(v, bf16x2_t); return __builtin_bit_cast(unsigned, b); }
; DI void p2_conv(Frame& F, int wk, int nwk) {
;     ...
;         for (int u = 0; u < 4; ++u) { const int tok = tokb + u * tstr; const int tc = tok < NTOK ? tok : NTOK - 1; const int t = tc & (SEQ - 1);
;             float a[8];
; #pragma unroll
;             for (int e = 0; e < 8; ++e) a[e] = cb[e];
; #pragma unroll
;             for (int j = 0; j < 4; ++j) { const float on_ = (t - 3 + j < 0) ? 0.0f : 1.0f;
; #pragma unroll
;                 for (int e = 0; e < 4; ++e) { a[2 * e] += __uint_as_float(raw[u][j][e] << 16) * (cw[j][2 * e] * on_); a[2 * e + 1] += __uint_as_float(raw[u][j][e] & 0xffff0000u) * (cw[j][2 * e + 1] * on_); } }
; #pragma unroll
;             for (int e = 0; e < 8; ++e) a[e] = a[e] * __builtin_amdgcn_rcpf(1.0f + __expf(-a[e])) * sc;
;             u32x4 w; w.x = cvtpk(a[0], a[1]); w.y = cvtpk(a[2], a[3]); w.z = cvtpk(a[4], a[5]); w.w = cvtpk(a[6], a[7]);
;             if (tok < NTOK) { if (c8 < 512) *(u32x4*)(QC + (size_t)tok * 512 + c8) = w; else *(u32x4*)(KC + (size_t)tok * 512 + (c8 - 512)) = w; } }
	v_and_b32_e32 v55, 0xffff0000, v94
	v_cndmask_b32_e64 v126, 0, 1.0, s[10:11]
	v_cndmask_b32_e64 v122, 1.0, 0, vcc
	v_cmp_gt_u32_e32 vcc, 2, v54
	v_lshlrev_b32_e32 v54, 16, v94
	v_pk_mul_f32 v[56:57], v[14:15], v[122:123] op_sel_hi:[1,0]
	v_cndmask_b32_e64 v124, 1.0, 0, vcc
	v_pk_fma_f32 v[54:55], v[56:57], v[54:55], v[10:11]
	s_waitcnt vmcnt(10)
	v_lshlrev_b32_e32 v56, 16, v90
	v_and_b32_e32 v57, 0xffff0000, v90
	v_pk_mul_f32 v[128:129], v[18:19], v[124:125] op_sel_hi:[1,0]
	v_lshl_add_u64 v[50:51], v[50:51], 0, v[106:107]
	v_pk_fma_f32 v[54:55], v[128:129], v[56:57], v[54:55]
	s_waitcnt vmcnt(9)
	v_lshlrev_b32_e32 v56, 16, v102
	v_and_b32_e32 v57, 0xffff0000, v102
	v_pk_mul_f32 v[128:129], v[22:23], v[126:127] op_sel_hi:[1,0]
	v_add_co_u32_e32 v50, vcc, s26, v50
	v_pk_fma_f32 v[54:55], v[128:129], v[56:57], v[54:55]
	s_waitcnt vmcnt(8)
	v_lshlrev_b32_e32 v56, 16, v98
	v_and_b32_e32 v57, 0xffff0000, v98
	v_pk_fma_f32 v[128:129], v[34:35], v[56:57], v[54:55]
	v_addc_co_u32_e32 v51, vcc, 0, v51, vcc
	v_mul_f32_e32 v54, 0xbfb8aa3b, v128
	v_exp_f32_e32 v54, v54
	v_mul_f32_e32 v55, 0xbfb8aa3b, v129
	v_exp_f32_e32 v55, v55
	global_load_dwordx4 v[46:49], v[42:43], off offset:2048 nt
	s_nop 0
	global_load_dwordx4 v[42:45], v[44:45], off offset:2048 nt
	v_add_f32_e32 v54, 1.0, v54
	v_rcp_f32_e32 v130, v54
	v_add_f32_e32 v54, 1.0, v55
	v_rcp_f32_e32 v131, v54
	global_load_dwordx4 v[54:57], v[52:53], off offset:2048 nt
	s_nop 0
	global_load_dwordx4 v[50:53], v[50:51], off offset:2048 nt
	v_lshlrev_b32_e32 v94, 16, v95
	v_and_b32_e32 v95, 0xffff0000, v95
	v_pk_mul_f32 v[128:129], v[128:129], v[130:131]
	v_pk_mul_f32 v[130:131], v[16:17], v[122:123] op_sel_hi:[1,0]
	v_lshlrev_b32_e32 v90, 16, v91
	v_pk_fma_f32 v[94:95], v[130:131], v[94:95], v[12:13]
	v_and_b32_e32 v91, 0xffff0000, v91
	v_pk_mul_f32 v[130:131], v[20:21], v[124:125] op_sel_hi:[1,0]
	v_ashrrev_i32_e32 v121, 31, v120
	v_pk_fma_f32 v[90:91], v[130:131], v[90:91], v[94:95]
	v_lshlrev_b32_e32 v94, 16, v103
	v_and_b32_e32 v95, 0xffff0000, v103
	v_pk_mul_f32 v[102:103], v[24:25], v[126:127] op_sel_hi:[1,0]
	v_pk_mul_f32 v[130:131], v[26:27], v[124:125] op_sel_hi:[1,0]
	v_pk_fma_f32 v[90:91], v[102:103], v[94:95], v[90:91]
	v_lshlrev_b32_e32 v94, 16, v99
	v_and_b32_e32 v95, 0xffff0000, v99
	v_pk_fma_f32 v[90:91], v[36:37], v[94:95], v[90:91]
	v_lshlrev_b32_e32 v102, 16, v96
	v_mul_f32_e32 v94, 0xbfb8aa3b, v90
	v_exp_f32_e32 v98, v94
	v_mul_f32_e32 v94, 0xbfb8aa3b, v91
	v_exp_f32_e32 v99, v94
	v_pk_mul_f32 v[94:95], v[108:109], v[128:129]
	v_and_b32_e32 v103, 0xffff0000, v96
	v_pk_mul_f32 v[128:129], v[6:7], v[122:123] op_sel_hi:[1,0]
	v_add_f32_e32 v98, 1.0, v98
	v_pk_fma_f32 v[102:103], v[128:129], v[102:103], v[2:3]
	v_lshlrev_b32_e32 v128, 16, v92
	v_and_b32_e32 v129, 0xffff0000, v92
	v_pk_fma_f32 v[102:103], v[130:131], v[128:129], v[102:103]
	v_lshlrev_b32_e32 v128, 16, v104
	v_and_b32_e32 v129, 0xffff0000, v104
	v_pk_mul_f32 v[130:131], v[30:31], v[126:127] op_sel_hi:[1,0]
	v_add_f32_e32 v99, 1.0, v99
	v_pk_fma_f32 v[102:103], v[130:131], v[128:129], v[102:103]
	v_lshlrev_b32_e32 v128, 16, v100
	v_and_b32_e32 v129, 0xffff0000, v100
	v_pk_fma_f32 v[102:103], v[38:39], v[128:129], v[102:103]
	v_rcp_f32_e32 v98, v98
	v_mul_f32_e32 v96, 0xbfb8aa3b, v103
	v_rcp_f32_e32 v99, v99
	v_exp_f32_e32 v96, v96
	v_mul_f32_e32 v92, 0xbfb8aa3b, v102
	v_exp_f32_e32 v92, v92
	v_pk_mul_f32 v[90:91], v[90:91], v[98:99]
	v_add_f32_e32 v100, 1.0, v96
	v_lshlrev_b32_e32 v96, 16, v97
	v_and_b32_e32 v97, 0xffff0000, v97
	v_pk_mul_f32 v[98:99], v[8:9], v[122:123] op_sel_hi:[1,0]
	v_pk_mul_f32 v[122:123], v[28:29], v[124:125] op_sel_hi:[1,0]
	v_pk_fma_f32 v[96:97], v[98:99], v[96:97], v[4:5]
	v_lshlrev_b32_e32 v98, 16, v93
	v_and_b32_e32 v99, 0xffff0000, v93
	v_pk_fma_f32 v[96:97], v[122:123], v[98:99], v[96:97]
	v_lshlrev_b32_e32 v98, 16, v105
	v_and_b32_e32 v99, 0xffff0000, v105
	v_pk_mul_f32 v[104:105], v[32:33], v[126:127] op_sel_hi:[1,0]
	v_add_f32_e32 v92, 1.0, v92
	v_pk_fma_f32 v[96:97], v[104:105], v[98:99], v[96:97]
	v_lshlrev_b32_e32 v98, 16, v101
	v_and_b32_e32 v99, 0xffff0000, v101
	v_pk_fma_f32 v[96:97], v[40:41], v[98:99], v[96:97]
	v_rcp_f32_e32 v92, v92
	v_mul_f32_e32 v93, 0xbfb8aa3b, v96
	v_exp_f32_e32 v98, v93
	v_mul_f32_e32 v93, 0xbfb8aa3b, v97
	v_exp_f32_e32 v99, v93
	v_rcp_f32_e32 v93, v100
	v_add_f32_e32 v98, 1.0, v98
	v_rcp_f32_e32 v98, v98
	v_add_f32_e32 v99, 1.0, v99
	v_rcp_f32_e32 v99, v99
	v_pk_mul_f32 v[100:101], v[108:109], v[90:91]
	v_pk_mul_f32 v[90:91], v[102:103], v[92:93]
	s_nop 0
	v_pk_mul_f32 v[92:93], v[108:109], v[90:91]
	v_pk_mul_f32 v[90:91], v[96:97], v[98:99]
	v_cvt_pk_bf16_f32 v92, v92, v93
	v_pk_mul_f32 v[96:97], v[108:109], v[90:91]
	v_cvt_pk_bf16_f32 v90, v94, v95
	v_cvt_pk_bf16_f32 v91, v100, v101
	v_cvt_pk_bf16_f32 v93, v96, v97
	v_lshlrev_b64 v[94:95], 10, v[120:121]
	s_and_saveexec_b64 s[0:1], s[2:3]
	s_xor_b64 s[0:1], exec, s[0:1]
	s_cbranch_execnz .LBB0_236
	s_andn2_saveexec_b64 s[0:1], s[0:1]
	s_cbranch_execnz .LBB0_237

; #define EPS_LOAD(g_) do { const size_t off_ = (size_t)(row0 + ((g_) >> 2) * HALF + ((g_) & 3) * 16) * ldc + col0; \
;             _Pragma("unroll") for (int bj = 0; bj < 2; ++bj) _Pragma("unroll") for (int n = 0; n < 2; ++n) rb[(g_) & 3][2 * bj + n] = *(const f32x4*)(base + off_ + bj * HALF + n * 16); } while (0)
;     DI void operator()(const f32x4 (&acc)[2][2][4][2], const Unit& u, int wr, int wc, int fr, int fq, const LAS unsigned char* st) const {
;         const int row0 = u.pm * BM + wr * 64 + fr, col0 = u.pn * BM + wc * 32 + 4 * fq;
;         f32x4 rb[4][4];
;     ...
;         EPS_LOAD(0); EPS_LOAD(1); EPS_LOAD(2);
; #pragma unroll
;         for (int ai = 0; ai < 2; ++ai)
; #pragma unroll
;             for (int m = 0; m < 4; ++m) { const int g = 4 * ai + m; const size_t off = (size_t)(row0 + ai * HALF + m * 16) * ldc + col0;
;                 if (g + 3 < 8) EPS_LOAD(g + 3);
; #pragma unroll
;                 for (int bj = 0; bj < 2; ++bj)
; #pragma unroll
;                     for (int n = 0; n < 2; ++n) *(f32x4*)(C + off + bj * HALF + n * 16) = rb[g & 3][2 * bj + n] + acc[ai][bj][m][n]; }
.LBB0_796:
	v_mov_b32_e32 v130, v224
	s_lshl_b32 s0, s28, 8
	s_add_i32 s0, s0, s45
	v_and_or_b32 v140, v130, 15, s0
	s_lshl_b32 s0, s54, 8
	v_ashrrev_i32_e32 v130, 2, v130
	s_or_b32 s0, s0, s46
	v_and_b32_e32 v130, -4, v130
	v_add_u32_e32 v136, s0, v130
	v_ashrrev_i32_e32 v141, 31, v140
	v_readlane_b32 s0, v254, 3
	v_or_b32_e32 v168, 16, v140
	v_or_b32_e32 v184, 32, v140
	v_ashrrev_i32_e32 v137, 31, v136
	v_lshlrev_b64 v[138:139], 13, v[140:141]
	v_readlane_b32 s1, v254, 4
	v_ashrrev_i32_e32 v169, 31, v168
	v_ashrrev_i32_e32 v185, 31, v184
	v_lshl_add_u64 v[152:153], s[0:1], 0, v[138:139]
	v_lshlrev_b64 v[136:137], 2, v[136:137]
	v_lshlrev_b64 v[216:217], 13, v[168:169]
	v_lshlrev_b64 v[218:219], 13, v[184:185]
	v_lshl_add_u64 v[164:165], v[152:153], 0, v[136:137]
	v_lshl_add_u64 v[168:169], s[0:1], 0, v[216:217]
	v_lshl_add_u64 v[184:185], s[0:1], 0, v[218:219]
	global_load_dwordx4 v[152:155], v[164:165], off nt
	global_load_dwordx4 v[156:159], v[164:165], off offset:64 nt
	global_load_dwordx4 v[160:163], v[164:165], off offset:512 nt
	s_nop 0
	global_load_dwordx4 v[164:167], v[164:165], off offset:576 nt
	v_lshl_add_u64 v[180:181], v[168:169], 0, v[136:137]
	v_lshl_add_u64 v[196:197], v[184:185], 0, v[136:137]
	global_load_dwordx4 v[168:171], v[180:181], off nt
	global_load_dwordx4 v[172:175], v[180:181], off offset:64 nt
	global_load_dwordx4 v[176:179], v[180:181], off offset:512 nt
	s_nop 0
	global_load_dwordx4 v[180:183], v[180:181], off offset:576 nt
	s_nop 0
	global_load_dwordx4 v[184:187], v[196:197], off nt
	global_load_dwordx4 v[188:191], v[196:197], off offset:64 nt
	global_load_dwordx4 v[192:195], v[196:197], off offset:512 nt
	s_nop 0
	global_load_dwordx4 v[196:199], v[196:197], off offset:576 nt
	v_or_b32_e32 v200, 48, v140
	v_ashrrev_i32_e32 v201, 31, v200
	v_lshlrev_b64 v[220:221], 13, v[200:201]
	v_lshl_add_u64 v[200:201], s[0:1], 0, v[220:221]
	v_lshl_add_u64 v[212:213], v[200:201], 0, v[136:137]
	global_load_dwordx4 v[200:203], v[212:213], off nt
	global_load_dwordx4 v[204:207], v[212:213], off offset:64 nt
	global_load_dwordx4 v[208:211], v[212:213], off offset:512 nt
	s_nop 0
	global_load_dwordx4 v[212:215], v[212:213], off offset:576 nt
	v_lshl_add_u64 v[222:223], s[92:93], 0, v[138:139]
	v_lshl_add_u64 v[226:227], v[138:139], 0, s[74:75]
	v_lshl_add_u64 v[228:229], v[138:139], 0, s[76:77]
	v_lshl_add_u64 v[230:231], s[0:1], 0, v[226:227]
	v_lshl_add_u64 v[216:217], s[92:93], 0, v[216:217]
	v_lshl_add_u64 v[138:139], v[222:223], 0, v[136:137]
	v_lshl_add_u64 v[232:233], s[0:1], 0, v[228:229]
	v_lshl_add_u64 v[218:219], s[92:93], 0, v[218:219]
	v_lshl_add_u64 v[222:223], v[230:231], 0, v[136:137]
	v_lshl_add_u64 v[216:217], v[216:217], 0, v[136:137]
	v_lshl_add_u64 v[230:231], v[232:233], 0, v[136:137]
	v_readlane_b32 s2, v254, 5
	v_readlane_b32 s3, v254, 6
	v_readlane_b32 s4, v254, 7
	v_readlane_b32 s5, v254, 8
	v_readlane_b32 s6, v254, 9
	v_readlane_b32 s7, v254, 10
	v_readlane_b32 s8, v254, 11
	v_readlane_b32 s9, v254, 12
	v_readlane_b32 s10, v254, 13
	v_readlane_b32 s11, v254, 14
	v_readlane_b32 s12, v254, 15
	v_readlane_b32 s13, v254, 16
	v_readlane_b32 s14, v254, 17
	v_readlane_b32 s15, v254, 18
	s_waitcnt vmcnt(0)
	v_pk_add_f32 v[128:129], v[128:129], v[154:155]
	v_pk_add_f32 v[126:127], v[126:127], v[152:153]
	v_pk_add_f32 v[124:125], v[124:125], v[158:159]
	v_pk_add_f32 v[122:123], v[122:123], v[156:157]
	v_pk_add_f32 v[108:109], v[108:109], v[162:163]
	v_pk_add_f32 v[106:107], v[106:107], v[160:161]
	v_pk_add_f32 v[104:105], v[104:105], v[166:167]
	v_pk_add_f32 v[102:103], v[102:103], v[164:165]
	v_pk_add_f32 v[120:121], v[120:121], v[170:171]
	v_pk_add_f32 v[118:119], v[118:119], v[168:169]
	global_store_dwordx4 v[138:139], v[126:129], off
	global_store_dwordx4 v[138:139], v[122:125], off offset:64
	global_store_dwordx4 v[138:139], v[106:109], off offset:512
	global_store_dwordx4 v[138:139], v[102:105], off offset:576
	v_pk_add_f32 v[116:117], v[116:117], v[174:175]
	v_pk_add_f32 v[114:115], v[114:115], v[172:173]
	v_pk_add_f32 v[100:101], v[100:101], v[178:179]
	v_pk_add_f32 v[98:99], v[98:99], v[176:177]
	v_pk_add_f32 v[96:97], v[96:97], v[182:183]
	v_pk_add_f32 v[94:95], v[94:95], v[180:181]
	global_load_dwordx4 v[102:105], v[222:223], off nt
	global_load_dwordx4 v[106:109], v[222:223], off offset:64 nt
	global_load_dwordx4 v[122:125], v[222:223], off offset:512 nt
	global_load_dwordx4 v[126:129], v[222:223], off offset:576 nt
	s_nop 0
	global_store_dwordx4 v[216:217], v[118:121], off
	global_store_dwordx4 v[216:217], v[114:117], off offset:64
	global_store_dwordx4 v[216:217], v[98:101], off offset:512
	global_store_dwordx4 v[216:217], v[94:97], off offset:576
	v_lshl_add_u64 v[152:153], v[218:219], 0, v[136:137]
	v_pk_add_f32 v[80:81], v[80:81], v[198:199]
	v_pk_add_f32 v[78:79], v[78:79], v[196:197]
	global_load_dwordx4 v[94:97], v[230:231], off nt
	global_load_dwordx4 v[98:101], v[230:231], off offset:64 nt
	global_load_dwordx4 v[114:117], v[230:231], off offset:512 nt
	global_load_dwordx4 v[118:121], v[230:231], off offset:576 nt
	v_pk_add_f32 v[112:113], v[112:113], v[186:187]
; #define EPS_LOAD(g_) do { const size_t off_ = (size_t)(row0 + ((g_) >> 2) * HALF + ((g_) & 3) * 16) * ldc + col0; \
;             _Pragma("unroll") for (int bj = 0; bj < 2; ++bj) _Pragma("unroll") for (int n = 0; n < 2; ++n) rb[(g_) & 3][2 * bj + n] = *(const f32x4*)(base + off_ + bj * HALF + n * 16); } while (0)
;     DI void operator()(const f32x4 (&acc)[2][2][4][2], const Unit& u, int wr, int wc, int fr, int fq, const LAS unsigned char* st) const {
;         const int row0 = u.pm * BM + wr * 64 + fr, col0 = u.pn * BM + wc * 32 + 4 * fq;
;         f32x4 rb[4][4];
;     ...
;         EPS_LOAD(0); EPS_LOAD(1); EPS_LOAD(2);
; #pragma unroll
;         for (int ai = 0; ai < 2; ++ai)
; #pragma unroll
;             for (int m = 0; m < 4; ++m) { const int g = 4 * ai + m; const size_t off = (size_t)(row0 + ai * HALF + m * 16) * ldc + col0;
;                 if (g + 3 < 8) EPS_LOAD(g + 3);
; #pragma unroll
;                 for (int bj = 0; bj < 2; ++bj)
; #pragma unroll
;                     for (int n = 0; n < 2; ++n) *(f32x4*)(C + off + bj * HALF + n * 16) = rb[g & 3][2 * bj + n] + acc[ai][bj][m][n]; }
	global_store_dwordx4 v[152:153], v[78:81], off offset:576
	v_pk_add_f32 v[110:111], v[110:111], v[184:185]
	v_pk_add_f32 v[92:93], v[92:93], v[190:191]
	v_add_u32_e32 v78, 0xa0, v140
	v_ashrrev_i32_e32 v79, 31, v78
	v_pk_add_f32 v[90:91], v[90:91], v[188:189]
	v_pk_add_f32 v[88:89], v[88:89], v[194:195]
	v_pk_add_f32 v[86:87], v[86:87], v[192:193]
	v_lshlrev_b64 v[78:79], 13, v[78:79]
	global_store_dwordx4 v[152:153], v[110:113], off
	global_store_dwordx4 v[152:153], v[90:93], off offset:64
	global_store_dwordx4 v[152:153], v[86:89], off offset:512
	v_lshl_add_u64 v[78:79], s[0:1], 0, v[78:79]
	v_lshl_add_u64 v[152:153], s[92:93], 0, v[220:221]
	v_lshl_add_u64 v[110:111], v[78:79], 0, v[136:137]
	v_lshl_add_u64 v[152:153], v[152:153], 0, v[136:137]
	v_pk_add_f32 v[68:69], v[68:69], v[214:215]
	v_pk_add_f32 v[66:67], v[66:67], v[212:213]
	global_load_dwordx4 v[78:81], v[110:111], off nt
	global_load_dwordx4 v[86:89], v[110:111], off offset:64 nt
	global_load_dwordx4 v[90:93], v[110:111], off offset:512 nt
	s_nop 0
	global_load_dwordx4 v[110:113], v[110:111], off offset:576 nt
	v_pk_add_f32 v[84:85], v[84:85], v[202:203]
	global_store_dwordx4 v[152:153], v[66:69], off offset:576
	v_pk_add_f32 v[82:83], v[82:83], v[200:201]
	v_pk_add_f32 v[76:77], v[76:77], v[206:207]
	v_add_u32_e32 v66, 0xb0, v140
	v_ashrrev_i32_e32 v67, 31, v66
	v_lshlrev_b64 v[66:67], 13, v[66:67]
	v_pk_add_f32 v[74:75], v[74:75], v[204:205]
	v_pk_add_f32 v[72:73], v[72:73], v[210:211]
	v_pk_add_f32 v[70:71], v[70:71], v[208:209]
	v_lshl_add_u64 v[66:67], s[0:1], 0, v[66:67]
	global_store_dwordx4 v[152:153], v[82:85], off
	global_store_dwordx4 v[152:153], v[74:77], off offset:64
	global_store_dwordx4 v[152:153], v[70:73], off offset:512
	v_lshl_add_u64 v[82:83], v[66:67], 0, v[136:137]
	global_load_dwordx4 v[66:69], v[82:83], off nt
	global_load_dwordx4 v[70:73], v[82:83], off offset:64 nt
	global_load_dwordx4 v[74:77], v[82:83], off offset:512 nt
	s_nop 0
	global_load_dwordx4 v[82:85], v[82:83], off offset:576 nt
	v_lshl_add_u64 v[140:141], s[92:93], 0, v[226:227]
	v_lshl_add_u64 v[152:153], s[92:93], 0, v[228:229]
	v_lshl_add_u64 v[140:141], v[140:141], 0, v[136:137]
	v_lshl_add_u64 v[136:137], v[152:153], 0, v[136:137]
	v_add_co_u32_e32 v154, vcc, s52, v138
	v_lshl_add_u64 v[152:153], v[138:139], 0, s[16:17]
	s_nop 0
	v_addc_co_u32_e32 v155, vcc, 0, v139, vcc
	s_mov_b64 s[0:1], -1
	s_waitcnt vmcnt(27)
	v_pk_add_f32 v[64:65], v[64:65], v[104:105]
	v_pk_add_f32 v[62:63], v[62:63], v[102:103]
	s_waitcnt vmcnt(26)
	v_pk_add_f32 v[60:61], v[60:61], v[108:109]
	s_waitcnt vmcnt(24)
	v_pk_add_f32 v[40:41], v[40:41], v[128:129]
	v_pk_add_f32 v[38:39], v[38:39], v[126:127]
	v_pk_add_f32 v[58:59], v[58:59], v[106:107]
	v_pk_add_f32 v[48:49], v[48:49], v[124:125]
	v_pk_add_f32 v[46:47], v[46:47], v[122:123]
	global_store_dwordx4 v[140:141], v[62:65], off
	global_store_dwordx4 v[140:141], v[58:61], off offset:64
	global_store_dwordx4 v[140:141], v[46:49], off offset:512
	global_store_dwordx4 v[140:141], v[38:41], off offset:576
	s_waitcnt vmcnt(20)
	v_pk_add_f32 v[28:29], v[28:29], v[120:121]
	v_pk_add_f32 v[26:27], v[26:27], v[118:119]
	v_pk_add_f32 v[40:41], v[56:57], v[96:97]
	v_pk_add_f32 v[38:39], v[54:55], v[94:95]
	v_pk_add_f32 v[48:49], v[52:53], v[100:101]
	v_pk_add_f32 v[46:47], v[50:51], v[98:99]
	v_pk_add_f32 v[32:33], v[32:33], v[116:117]
	v_pk_add_f32 v[30:31], v[30:31], v[114:115]
	global_store_dwordx4 v[136:137], v[38:41], off
	global_store_dwordx4 v[136:137], v[46:49], off offset:64
	global_store_dwordx4 v[136:137], v[30:33], off offset:512
	global_store_dwordx4 v[136:137], v[26:29], off offset:576
	s_waitcnt vmcnt(17)
	v_pk_add_f32 v[20:21], v[20:21], v[92:93]
	v_pk_add_f32 v[28:29], v[44:45], v[80:81]
	v_pk_add_f32 v[26:27], v[42:43], v[78:79]
	v_pk_add_f32 v[18:19], v[18:19], v[90:91]
	v_pk_add_f32 v[32:33], v[36:37], v[88:89]
	v_pk_add_f32 v[30:31], v[34:35], v[86:87]
	global_store_dwordx4 v[154:155], v[26:29], off
	global_store_dwordx4 v[152:153], v[30:33], off offset:64
	global_store_dwordx4 v[152:153], v[18:21], off offset:512
	s_waitcnt vmcnt(19)
	v_pk_add_f32 v[16:17], v[16:17], v[112:113]
	v_pk_add_f32 v[14:15], v[14:15], v[110:111]
	v_add_co_u32_e32 v20, vcc, s53, v138
	global_store_dwordx4 v[152:153], v[14:17], off offset:576
	s_nop 0
	v_addc_co_u32_e32 v21, vcc, 0, v139, vcc
	s_waitcnt vmcnt(15)
	v_pk_add_f32 v[16:17], v[24:25], v[68:69]
	v_pk_add_f32 v[14:15], v[22:23], v[66:67]
	v_lshl_add_u64 v[18:19], v[138:139], 0, s[18:19]
	s_waitcnt vmcnt(14)
	v_pk_add_f32 v[12:13], v[12:13], v[72:73]
	v_pk_add_f32 v[10:11], v[10:11], v[70:71]
	s_waitcnt vmcnt(13)
	v_pk_add_f32 v[8:9], v[8:9], v[76:77]
	v_pk_add_f32 v[6:7], v[6:7], v[74:75]
	s_waitcnt vmcnt(12)
	v_pk_add_f32 v[4:5], v[4:5], v[84:85]
	v_pk_add_f32 v[2:3], v[2:3], v[82:83]
	s_andn2_b64 vcc, exec, s[60:61]
	global_store_dwordx4 v[20:21], v[14:17], off
	global_store_dwordx4 v[18:19], v[10:13], off offset:64
	global_store_dwordx4 v[18:19], v[6:9], off offset:512
	global_store_dwordx4 v[18:19], v[2:5], off offset:576
	s_cbranch_vccnz .LBB0_785
	s_andn2_b64 vcc, exec, s[64:65]
	s_cbranch_vccnz .LBB0_784
	s_barrier
	s_branch .LBB0_784
